# speedup vs baseline: 1.0054x; 1.0054x over previous
.Lg1_w03:
	v_and_b32_e32 v98, 15, v0
	v_bfe_u32 v97, v0, 4, 2
	v_lshrrev_b32_e32 v96, 7, v0
	v_bfe_u32 v1, v0, 6, 1
	v_bfe_u32 v95, v0, 1, 3
	v_xor_b32_e32 v95, v97, v95
	v_lshlrev_b32_e32 v95, 4, v95
	v_lshl_or_b32 v99, v98, 7, v95
	v_lshl_or_b32 v89, v96, 13, v99
	v_mul_u32_u24_e32 v95, 0x2800, v1
	v_add_u32_e32 v95, 0x8000, v95
	v_add_u32_e32 v90, v95, v99
	s_waitcnt lgkmcnt(0)
	s_mov_b32 s22, s12
	s_mov_b32 s23, s13
	s_mov_b32 s24, s14
	s_mov_b32 s25, s15
	s_mov_b32 s26, s20
	s_add_i32 s30, s26, s29
	s_mov_b32 m0, s26
	s_add_i32 s26, s26, 0x2000
	global_load_lds_dwordx4 v82, s[22:23]
	s_mov_b32 m0, s26
	s_add_i32 s26, s26, 0x2000
	global_load_lds_dwordx4 v83, s[22:23]
	s_mov_b32 m0, s26
	s_add_i32 s26, s26, 0x2000
	global_load_lds_dwordx4 v84, s[22:23]
	s_mov_b32 m0, s26
	s_add_i32 s26, s26, 0x2000
	global_load_lds_dwordx4 v85, s[22:23]
	s_mov_b32 m0, s26
	s_add_i32 s26, s26, 0x2000
	global_load_lds_dwordx4 v86, s[24:25]
	s_mov_b32 m0, s26
	s_add_i32 s26, s26, 0x2000
	global_load_lds_dwordx4 v87, s[24:25]
	s_mov_b32 m0, s30
	s_add_i32 s26, s26, 0x1000
	global_load_lds_dwordx4 v88, s[24:25]
	s_add_u32 s22, s22, 0x80
	s_addc_u32 s23, s23, 0
	s_add_u32 s24, s24, 0x80
	s_addc_u32 s25, s25, 0
	s_add_i32 s30, s26, s29
	s_mov_b32 m0, s26
	s_add_i32 s26, s26, 0x2000
	global_load_lds_dwordx4 v82, s[22:23]
	s_mov_b32 m0, s26
	s_add_i32 s26, s26, 0x2000
	global_load_lds_dwordx4 v83, s[22:23]
	s_mov_b32 m0, s26
	s_add_i32 s26, s26, 0x2000
	global_load_lds_dwordx4 v84, s[22:23]
	s_mov_b32 m0, s26
	s_add_i32 s26, s26, 0x2000
	global_load_lds_dwordx4 v85, s[22:23]
	s_mov_b32 m0, s26
	s_add_i32 s26, s26, 0x2000
	global_load_lds_dwordx4 v86, s[24:25]
	s_mov_b32 m0, s26
	s_add_i32 s26, s26, 0x2000
	global_load_lds_dwordx4 v87, s[24:25]
	s_mov_b32 m0, s30
	s_add_i32 s26, s26, 0x1000
	global_load_lds_dwordx4 v88, s[24:25]
	s_add_u32 s22, s22, 0x80
	s_addc_u32 s23, s23, 0
	s_add_u32 s24, s24, 0x80
	s_addc_u32 s25, s25, 0
	s_add_i32 s30, s26, s29
	s_mov_b32 m0, s26
	s_add_i32 s26, s26, 0x2000
	global_load_lds_dwordx4 v82, s[22:23]
	s_mov_b32 m0, s26
	s_add_i32 s26, s26, 0x2000
	global_load_lds_dwordx4 v83, s[22:23]
	s_mov_b32 m0, s26
	s_add_i32 s26, s26, 0x2000
	global_load_lds_dwordx4 v84, s[22:23]
	s_mov_b32 m0, s26
	s_add_i32 s26, s26, 0x2000
	global_load_lds_dwordx4 v85, s[22:23]
	s_mov_b32 m0, s26
	s_add_i32 s26, s26, 0x2000
	global_load_lds_dwordx4 v86, s[24:25]
	s_mov_b32 m0, s26
	s_add_i32 s26, s26, 0x2000
	global_load_lds_dwordx4 v87, s[24:25]
	s_mov_b32 m0, s30
	s_add_i32 s26, s26, 0x1000
	global_load_lds_dwordx4 v88, s[24:25]
	v_mov_b32_e32 v2, 0
	v_mov_b32_e32 v3, 0
	v_mov_b32_e32 v4, 0
	v_mov_b32_e32 v5, 0
	v_mov_b32_e32 v6, 0
	v_mov_b32_e32 v7, 0
	v_mov_b32_e32 v8, 0
	v_mov_b32_e32 v9, 0
	v_mov_b32_e32 v10, 0
	v_mov_b32_e32 v11, 0
	v_mov_b32_e32 v12, 0
	v_mov_b32_e32 v13, 0
	v_mov_b32_e32 v14, 0
	v_mov_b32_e32 v15, 0
	v_mov_b32_e32 v16, 0
	v_mov_b32_e32 v17, 0
	v_mov_b32_e32 v18, 0
	v_mov_b32_e32 v19, 0
	v_mov_b32_e32 v20, 0
	v_mov_b32_e32 v21, 0
	v_mov_b32_e32 v22, 0
	v_mov_b32_e32 v23, 0
	v_mov_b32_e32 v24, 0
	v_mov_b32_e32 v25, 0
	v_mov_b32_e32 v26, 0
	v_mov_b32_e32 v27, 0
	v_mov_b32_e32 v28, 0
	v_mov_b32_e32 v29, 0
	v_mov_b32_e32 v30, 0
	v_mov_b32_e32 v31, 0
	v_mov_b32_e32 v32, 0
	v_mov_b32_e32 v33, 0
	v_mov_b32_e32 v34, 0
	v_mov_b32_e32 v35, 0
	v_mov_b32_e32 v36, 0
	v_mov_b32_e32 v37, 0
	v_mov_b32_e32 v38, 0
	v_mov_b32_e32 v39, 0
	v_mov_b32_e32 v40, 0
	v_mov_b32_e32 v41, 0
	v_mov_b32_e32 v42, 0
	v_mov_b32_e32 v43, 0
	v_mov_b32_e32 v44, 0
	v_mov_b32_e32 v45, 0
	v_mov_b32_e32 v46, 0
	v_mov_b32_e32 v47, 0
	v_mov_b32_e32 v48, 0
	v_mov_b32_e32 v49, 0
	v_mov_b32_e32 v50, 0
	v_mov_b32_e32 v51, 0
	v_mov_b32_e32 v52, 0
	v_mov_b32_e32 v53, 0
	v_mov_b32_e32 v54, 0
	v_mov_b32_e32 v55, 0
	v_mov_b32_e32 v56, 0
	v_mov_b32_e32 v57, 0
	v_mov_b32_e32 v58, 0
	v_mov_b32_e32 v59, 0
	v_mov_b32_e32 v60, 0
	v_mov_b32_e32 v61, 0
	v_mov_b32_e32 v62, 0
	v_mov_b32_e32 v63, 0
	v_mov_b32_e32 v64, 0
	v_mov_b32_e32 v65, 0
	v_mov_b32_e32 v66, 0
	v_mov_b32_e32 v67, 0
	v_mov_b32_e32 v68, 0
	v_mov_b32_e32 v69, 0
	v_mov_b32_e32 v70, 0
	v_mov_b32_e32 v71, 0
	v_mov_b32_e32 v72, 0
	v_mov_b32_e32 v73, 0
	v_mov_b32_e32 v74, 0
	v_mov_b32_e32 v75, 0
	v_mov_b32_e32 v76, 0
	v_mov_b32_e32 v77, 0
	v_mov_b32_e32 v78, 0
	v_mov_b32_e32 v79, 0
	v_mov_b32_e32 v80, 0
	v_mov_b32_e32 v81, 0
	s_mov_b32 s16, 0
	s_mov_b32 s17, 0
	v_mov_b32_e32 v91, v89
	v_mov_b32_e32 v93, v90
	v_xor_b32_e32 v92, 64, v89
	v_xor_b32_e32 v94, 64, v90
	s_waitcnt vmcnt(14)
	s_barrier
	ds_read_b128 v[116:119], v93
	ds_read_b128 v[100:103], v91
	ds_read_b128 v[120:123], v93 offset:2048
	ds_read_b128 v[104:107], v91 offset:2048
	ds_read_b128 v[124:127], v93 offset:4096
	ds_read_b128 v[108:111], v91 offset:4096
	ds_read_b128 v[128:131], v93 offset:6144
	ds_read_b128 v[112:115], v91 offset:6144
	ds_read_b128 v[132:135], v93 offset:8192
	s_add_i32 s27, s17, 0xd000
	s_cmp_lg_u32 s27, 0x27000
	s_cselect_b32 s27, s27, 0
	s_waitcnt lgkmcnt(0)
	v_mfma_f32_16x16x32_f16 v[34:37], v[116:119], v[100:103], v[34:37]
	ds_read_b128 v[152:155], v94
	v_mfma_f32_16x16x32_f16 v[78:81], v[120:123], v[100:103], v[78:81]
	ds_read_b128 v[136:139], v92
	v_mfma_f32_16x16x32_f16 v[74:77], v[124:127], v[100:103], v[74:77]
	ds_read_b128 v[156:159], v94 offset:2048
	v_mfma_f32_16x16x32_f16 v[70:73], v[128:131], v[100:103], v[70:73]
	ds_read_b128 v[140:143], v92 offset:2048
	v_mfma_f32_16x16x32_f16 v[62:65], v[132:135], v[100:103], v[62:65]
	ds_read_b128 v[160:163], v94 offset:4096
	v_mfma_f32_16x16x32_f16 v[58:61], v[116:119], v[104:107], v[58:61]
	ds_read_b128 v[144:147], v92 offset:4096
	v_mfma_f32_16x16x32_f16 v[54:57], v[120:123], v[104:107], v[54:57]
	ds_read_b128 v[164:167], v94 offset:6144
	v_mfma_f32_16x16x32_f16 v[50:53], v[124:127], v[104:107], v[50:53]
	ds_read_b128 v[148:151], v92 offset:6144
	v_mfma_f32_16x16x32_f16 v[46:49], v[128:131], v[104:107], v[46:49]
	ds_read_b128 v[168:171], v94 offset:8192
	v_mfma_f32_16x16x32_f16 v[42:45], v[132:135], v[104:107], v[42:45]
	v_mfma_f32_16x16x32_f16 v[38:41], v[116:119], v[108:111], v[38:41]
	v_add_u32_e32 v91, s27, v89
	v_mfma_f32_16x16x32_f16 v[30:33], v[120:123], v[108:111], v[30:33]
	v_add_u32_e32 v93, s27, v90
	v_mfma_f32_16x16x32_f16 v[26:29], v[124:127], v[108:111], v[26:29]
	v_xor_b32_e32 v92, 64, v91
	v_mfma_f32_16x16x32_f16 v[22:25], v[128:131], v[108:111], v[22:25]
	v_xor_b32_e32 v94, 64, v93
	v_mfma_f32_16x16x32_f16 v[18:21], v[132:135], v[108:111], v[18:21]
	v_mfma_f32_16x16x32_f16 v[14:17], v[116:119], v[112:115], v[14:17]
	v_mfma_f32_16x16x32_f16 v[10:13], v[120:123], v[112:115], v[10:13]
	v_mfma_f32_16x16x32_f16 v[2:5], v[124:127], v[112:115], v[2:5]
	v_mfma_f32_16x16x32_f16 v[6:9], v[128:131], v[112:115], v[6:9]
	v_mfma_f32_16x16x32_f16 v[66:69], v[132:135], v[112:115], v[66:69]
	s_add_i32 s18, s16, 3
	s_lshl_b32 s18, s18, 7
	s_add_u32 s22, s12, s18
	s_addc_u32 s23, s13, 0
	s_add_u32 s24, s14, s18
	s_addc_u32 s25, s15, 0
	s_add_i32 s26, s17, s20
	s_add_i32 s30, s26, s29
	s_waitcnt vmcnt(7)
	s_waitcnt lgkmcnt(0)
	s_barrier
	v_mfma_f32_16x16x32_f16 v[34:37], v[152:155], v[136:139], v[34:37]
	ds_read_b128 v[116:119], v93
	v_mfma_f32_16x16x32_f16 v[78:81], v[156:159], v[136:139], v[78:81]
	ds_read_b128 v[100:103], v91
	v_mfma_f32_16x16x32_f16 v[74:77], v[160:163], v[136:139], v[74:77]
	ds_read_b128 v[120:123], v93 offset:2048
	v_mfma_f32_16x16x32_f16 v[70:73], v[164:167], v[136:139], v[70:73]
	ds_read_b128 v[104:107], v91 offset:2048
	v_mfma_f32_16x16x32_f16 v[62:65], v[168:171], v[136:139], v[62:65]
	ds_read_b128 v[124:127], v93 offset:4096
	v_mfma_f32_16x16x32_f16 v[58:61], v[152:155], v[140:143], v[58:61]
	ds_read_b128 v[108:111], v91 offset:4096
	v_mfma_f32_16x16x32_f16 v[54:57], v[156:159], v[140:143], v[54:57]
	ds_read_b128 v[128:131], v93 offset:6144
	v_mfma_f32_16x16x32_f16 v[50:53], v[160:163], v[140:143], v[50:53]
	ds_read_b128 v[112:115], v91 offset:6144
	v_mfma_f32_16x16x32_f16 v[46:49], v[164:167], v[140:143], v[46:49]
	ds_read_b128 v[132:135], v93 offset:8192
	v_mfma_f32_16x16x32_f16 v[42:45], v[168:171], v[140:143], v[42:45]
	v_mfma_f32_16x16x32_f16 v[38:41], v[152:155], v[144:147], v[38:41]
	s_mov_b32 m0, s26
	s_add_i32 s26, s26, 0x2000
	global_load_lds_dwordx4 v82, s[22:23]
	v_mfma_f32_16x16x32_f16 v[30:33], v[156:159], v[144:147], v[30:33]
	v_mfma_f32_16x16x32_f16 v[26:29], v[160:163], v[144:147], v[26:29]
	v_mfma_f32_16x16x32_f16 v[22:25], v[164:167], v[144:147], v[22:25]
	s_mov_b32 m0, s26
	s_add_i32 s26, s26, 0x2000
	global_load_lds_dwordx4 v83, s[22:23]
	v_mfma_f32_16x16x32_f16 v[18:21], v[168:171], v[144:147], v[18:21]
	v_mfma_f32_16x16x32_f16 v[14:17], v[152:155], v[148:151], v[14:17]
	v_mfma_f32_16x16x32_f16 v[10:13], v[156:159], v[148:151], v[10:13]
	s_mov_b32 m0, s26
	s_add_i32 s26, s26, 0x2000
	global_load_lds_dwordx4 v84, s[22:23]
	v_mfma_f32_16x16x32_f16 v[2:5], v[160:163], v[148:151], v[2:5]
	v_mfma_f32_16x16x32_f16 v[6:9], v[164:167], v[148:151], v[6:9]
	v_mfma_f32_16x16x32_f16 v[66:69], v[168:171], v[148:151], v[66:69]
	s_mov_b32 m0, s26
	s_add_i32 s26, s26, 0x2000
	global_load_lds_dwordx4 v85, s[22:23]
	s_mov_b32 s17, s27
	s_add_i32 s16, s16, 1
.Lg1_loop:
	s_add_i32 s27, s17, 0xd000
	s_cmp_lg_u32 s27, 0x27000
	s_cselect_b32 s27, s27, 0
	s_waitcnt lgkmcnt(0)
	v_mfma_f32_16x16x32_f16 v[34:37], v[116:119], v[100:103], v[34:37]
	ds_read_b128 v[152:155], v94
	v_mfma_f32_16x16x32_f16 v[78:81], v[120:123], v[100:103], v[78:81]
	ds_read_b128 v[136:139], v92
	v_mfma_f32_16x16x32_f16 v[74:77], v[124:127], v[100:103], v[74:77]
	ds_read_b128 v[156:159], v94 offset:2048
	v_mfma_f32_16x16x32_f16 v[70:73], v[128:131], v[100:103], v[70:73]
	ds_read_b128 v[140:143], v92 offset:2048
	v_mfma_f32_16x16x32_f16 v[62:65], v[132:135], v[100:103], v[62:65]
	ds_read_b128 v[160:163], v94 offset:4096
	v_mfma_f32_16x16x32_f16 v[58:61], v[116:119], v[104:107], v[58:61]
	ds_read_b128 v[144:147], v92 offset:4096
	v_mfma_f32_16x16x32_f16 v[54:57], v[120:123], v[104:107], v[54:57]
	ds_read_b128 v[164:167], v94 offset:6144
	v_mfma_f32_16x16x32_f16 v[50:53], v[124:127], v[104:107], v[50:53]
	ds_read_b128 v[148:151], v92 offset:6144
	v_mfma_f32_16x16x32_f16 v[46:49], v[128:131], v[104:107], v[46:49]
	ds_read_b128 v[168:171], v94 offset:8192
	v_mfma_f32_16x16x32_f16 v[42:45], v[132:135], v[104:107], v[42:45]
	v_mfma_f32_16x16x32_f16 v[38:41], v[116:119], v[108:111], v[38:41]
	v_add_u32_e32 v91, s27, v89
	v_mfma_f32_16x16x32_f16 v[30:33], v[120:123], v[108:111], v[30:33]
	v_add_u32_e32 v93, s27, v90
	v_mfma_f32_16x16x32_f16 v[26:29], v[124:127], v[108:111], v[26:29]
	v_xor_b32_e32 v92, 64, v91
	v_mfma_f32_16x16x32_f16 v[22:25], v[128:131], v[108:111], v[22:25]
	v_xor_b32_e32 v94, 64, v93
	v_mfma_f32_16x16x32_f16 v[18:21], v[132:135], v[108:111], v[18:21]
	s_mov_b32 m0, s26
	s_add_i32 s26, s26, 0x2000
	global_load_lds_dwordx4 v86, s[24:25]
	v_mfma_f32_16x16x32_f16 v[14:17], v[116:119], v[112:115], v[14:17]
	v_mfma_f32_16x16x32_f16 v[10:13], v[120:123], v[112:115], v[10:13]
	s_mov_b32 m0, s26
	s_nop 0
	global_load_lds_dwordx4 v87, s[24:25]
	v_mfma_f32_16x16x32_f16 v[2:5], v[124:127], v[112:115], v[2:5]
	v_mfma_f32_16x16x32_f16 v[6:9], v[128:131], v[112:115], v[6:9]
	s_mov_b32 m0, s30
	s_nop 0
	global_load_lds_dwordx4 v88, s[24:25]
	v_mfma_f32_16x16x32_f16 v[66:69], v[132:135], v[112:115], v[66:69]
	s_add_i32 s18, s16, 3
	s_lshl_b32 s18, s18, 7
	s_add_u32 s22, s12, s18
	s_addc_u32 s23, s13, 0
	s_add_u32 s24, s14, s18
	s_addc_u32 s25, s15, 0
	s_add_i32 s26, s17, s20
	s_add_i32 s30, s26, s29
	s_waitcnt vmcnt(7)
	s_waitcnt lgkmcnt(0)
	s_barrier
	v_mfma_f32_16x16x32_f16 v[34:37], v[152:155], v[136:139], v[34:37]
	ds_read_b128 v[116:119], v93
	v_mfma_f32_16x16x32_f16 v[78:81], v[156:159], v[136:139], v[78:81]
	ds_read_b128 v[100:103], v91
	v_mfma_f32_16x16x32_f16 v[74:77], v[160:163], v[136:139], v[74:77]
	ds_read_b128 v[120:123], v93 offset:2048
	v_mfma_f32_16x16x32_f16 v[70:73], v[164:167], v[136:139], v[70:73]
	ds_read_b128 v[104:107], v91 offset:2048
	v_mfma_f32_16x16x32_f16 v[62:65], v[168:171], v[136:139], v[62:65]
	ds_read_b128 v[124:127], v93 offset:4096
	v_mfma_f32_16x16x32_f16 v[58:61], v[152:155], v[140:143], v[58:61]
	ds_read_b128 v[108:111], v91 offset:4096
	v_mfma_f32_16x16x32_f16 v[54:57], v[156:159], v[140:143], v[54:57]
	ds_read_b128 v[128:131], v93 offset:6144
	v_mfma_f32_16x16x32_f16 v[50:53], v[160:163], v[140:143], v[50:53]
	ds_read_b128 v[112:115], v91 offset:6144
	v_mfma_f32_16x16x32_f16 v[46:49], v[164:167], v[140:143], v[46:49]
	ds_read_b128 v[132:135], v93 offset:8192
	v_mfma_f32_16x16x32_f16 v[42:45], v[168:171], v[140:143], v[42:45]
	v_mfma_f32_16x16x32_f16 v[38:41], v[152:155], v[144:147], v[38:41]
	s_mov_b32 m0, s26
	s_add_i32 s26, s26, 0x2000
	global_load_lds_dwordx4 v82, s[22:23]
	v_mfma_f32_16x16x32_f16 v[30:33], v[156:159], v[144:147], v[30:33]
	v_mfma_f32_16x16x32_f16 v[26:29], v[160:163], v[144:147], v[26:29]
	v_mfma_f32_16x16x32_f16 v[22:25], v[164:167], v[144:147], v[22:25]
	s_mov_b32 m0, s26
	s_add_i32 s26, s26, 0x2000
	global_load_lds_dwordx4 v83, s[22:23]
	v_mfma_f32_16x16x32_f16 v[18:21], v[168:171], v[144:147], v[18:21]
	v_mfma_f32_16x16x32_f16 v[14:17], v[152:155], v[148:151], v[14:17]
	v_mfma_f32_16x16x32_f16 v[10:13], v[156:159], v[148:151], v[10:13]
	s_mov_b32 m0, s26
	s_add_i32 s26, s26, 0x2000
	global_load_lds_dwordx4 v84, s[22:23]
	v_mfma_f32_16x16x32_f16 v[2:5], v[160:163], v[148:151], v[2:5]
	v_mfma_f32_16x16x32_f16 v[6:9], v[164:167], v[148:151], v[6:9]
	v_mfma_f32_16x16x32_f16 v[66:69], v[168:171], v[148:151], v[66:69]
	s_mov_b32 m0, s26
	s_add_i32 s26, s26, 0x2000
	global_load_lds_dwordx4 v85, s[22:23]
	s_mov_b32 s17, s27
	s_add_i32 s16, s16, 1
	s_cmp_lt_u32 s16, 13
	s_cbranch_scc1 .Lg1_loop
	s_add_i32 s27, s17, 0xd000
	s_cmp_lg_u32 s27, 0x27000
	s_cselect_b32 s27, s27, 0
	s_waitcnt lgkmcnt(0)
	v_mfma_f32_16x16x32_f16 v[34:37], v[116:119], v[100:103], v[34:37]
	ds_read_b128 v[152:155], v94
	v_mfma_f32_16x16x32_f16 v[78:81], v[120:123], v[100:103], v[78:81]
	ds_read_b128 v[136:139], v92
	v_mfma_f32_16x16x32_f16 v[74:77], v[124:127], v[100:103], v[74:77]
	ds_read_b128 v[156:159], v94 offset:2048
	v_mfma_f32_16x16x32_f16 v[70:73], v[128:131], v[100:103], v[70:73]
	ds_read_b128 v[140:143], v92 offset:2048
	v_mfma_f32_16x16x32_f16 v[62:65], v[132:135], v[100:103], v[62:65]
	ds_read_b128 v[160:163], v94 offset:4096
	v_mfma_f32_16x16x32_f16 v[58:61], v[116:119], v[104:107], v[58:61]
	ds_read_b128 v[144:147], v92 offset:4096
	v_mfma_f32_16x16x32_f16 v[54:57], v[120:123], v[104:107], v[54:57]
	ds_read_b128 v[164:167], v94 offset:6144
	v_mfma_f32_16x16x32_f16 v[50:53], v[124:127], v[104:107], v[50:53]
	ds_read_b128 v[148:151], v92 offset:6144
	v_mfma_f32_16x16x32_f16 v[46:49], v[128:131], v[104:107], v[46:49]
	ds_read_b128 v[168:171], v94 offset:8192
	v_mfma_f32_16x16x32_f16 v[42:45], v[132:135], v[104:107], v[42:45]
	v_mfma_f32_16x16x32_f16 v[38:41], v[116:119], v[108:111], v[38:41]
	v_add_u32_e32 v91, s27, v89
	v_mfma_f32_16x16x32_f16 v[30:33], v[120:123], v[108:111], v[30:33]
	v_add_u32_e32 v93, s27, v90
	v_mfma_f32_16x16x32_f16 v[26:29], v[124:127], v[108:111], v[26:29]
	v_xor_b32_e32 v92, 64, v91
	v_mfma_f32_16x16x32_f16 v[22:25], v[128:131], v[108:111], v[22:25]
	v_xor_b32_e32 v94, 64, v93
	v_mfma_f32_16x16x32_f16 v[18:21], v[132:135], v[108:111], v[18:21]
	s_mov_b32 m0, s26
	s_add_i32 s26, s26, 0x2000
	global_load_lds_dwordx4 v86, s[24:25]
	v_mfma_f32_16x16x32_f16 v[14:17], v[116:119], v[112:115], v[14:17]
	v_mfma_f32_16x16x32_f16 v[10:13], v[120:123], v[112:115], v[10:13]
	s_mov_b32 m0, s26
	s_nop 0
	global_load_lds_dwordx4 v87, s[24:25]
	v_mfma_f32_16x16x32_f16 v[2:5], v[124:127], v[112:115], v[2:5]
	v_mfma_f32_16x16x32_f16 v[6:9], v[128:131], v[112:115], v[6:9]
	s_mov_b32 m0, s30
	s_nop 0
	global_load_lds_dwordx4 v88, s[24:25]
	v_mfma_f32_16x16x32_f16 v[66:69], v[132:135], v[112:115], v[66:69]
	s_waitcnt vmcnt(7)
	s_waitcnt lgkmcnt(0)
	s_barrier
	v_mfma_f32_16x16x32_f16 v[34:37], v[152:155], v[136:139], v[34:37]
	ds_read_b128 v[116:119], v93
	v_mfma_f32_16x16x32_f16 v[78:81], v[156:159], v[136:139], v[78:81]
	ds_read_b128 v[100:103], v91
	v_mfma_f32_16x16x32_f16 v[74:77], v[160:163], v[136:139], v[74:77]
	ds_read_b128 v[120:123], v93 offset:2048
	v_mfma_f32_16x16x32_f16 v[70:73], v[164:167], v[136:139], v[70:73]
	ds_read_b128 v[104:107], v91 offset:2048
	v_mfma_f32_16x16x32_f16 v[62:65], v[168:171], v[136:139], v[62:65]
	ds_read_b128 v[124:127], v93 offset:4096
	v_mfma_f32_16x16x32_f16 v[58:61], v[152:155], v[140:143], v[58:61]
	ds_read_b128 v[108:111], v91 offset:4096
	v_mfma_f32_16x16x32_f16 v[54:57], v[156:159], v[140:143], v[54:57]
	ds_read_b128 v[128:131], v93 offset:6144
	v_mfma_f32_16x16x32_f16 v[50:53], v[160:163], v[140:143], v[50:53]
	ds_read_b128 v[112:115], v91 offset:6144
	v_mfma_f32_16x16x32_f16 v[46:49], v[164:167], v[140:143], v[46:49]
	ds_read_b128 v[132:135], v93 offset:8192
	v_mfma_f32_16x16x32_f16 v[42:45], v[168:171], v[140:143], v[42:45]
	v_mfma_f32_16x16x32_f16 v[38:41], v[152:155], v[144:147], v[38:41]
	v_mfma_f32_16x16x32_f16 v[30:33], v[156:159], v[144:147], v[30:33]
	v_mfma_f32_16x16x32_f16 v[26:29], v[160:163], v[144:147], v[26:29]
	v_mfma_f32_16x16x32_f16 v[22:25], v[164:167], v[144:147], v[22:25]
	v_mfma_f32_16x16x32_f16 v[18:21], v[168:171], v[144:147], v[18:21]
	v_mfma_f32_16x16x32_f16 v[14:17], v[152:155], v[148:151], v[14:17]
	v_mfma_f32_16x16x32_f16 v[10:13], v[156:159], v[148:151], v[10:13]
	v_mfma_f32_16x16x32_f16 v[2:5], v[160:163], v[148:151], v[2:5]
	v_mfma_f32_16x16x32_f16 v[6:9], v[164:167], v[148:151], v[6:9]
	v_mfma_f32_16x16x32_f16 v[66:69], v[168:171], v[148:151], v[66:69]
	s_mov_b32 s17, s27
	s_add_i32 s16, s16, 1
	s_add_i32 s27, s17, 0xd000
	s_cmp_lg_u32 s27, 0x27000
	s_cselect_b32 s27, s27, 0
	s_waitcnt lgkmcnt(0)
	v_mfma_f32_16x16x32_f16 v[34:37], v[116:119], v[100:103], v[34:37]
	ds_read_b128 v[152:155], v94
	v_mfma_f32_16x16x32_f16 v[78:81], v[120:123], v[100:103], v[78:81]
	ds_read_b128 v[136:139], v92
	v_mfma_f32_16x16x32_f16 v[74:77], v[124:127], v[100:103], v[74:77]
	ds_read_b128 v[156:159], v94 offset:2048
	v_mfma_f32_16x16x32_f16 v[70:73], v[128:131], v[100:103], v[70:73]
	ds_read_b128 v[140:143], v92 offset:2048
	v_mfma_f32_16x16x32_f16 v[62:65], v[132:135], v[100:103], v[62:65]
	ds_read_b128 v[160:163], v94 offset:4096
	v_mfma_f32_16x16x32_f16 v[58:61], v[116:119], v[104:107], v[58:61]
	ds_read_b128 v[144:147], v92 offset:4096
	v_mfma_f32_16x16x32_f16 v[54:57], v[120:123], v[104:107], v[54:57]
	ds_read_b128 v[164:167], v94 offset:6144
	v_mfma_f32_16x16x32_f16 v[50:53], v[124:127], v[104:107], v[50:53]
	ds_read_b128 v[148:151], v92 offset:6144
	v_mfma_f32_16x16x32_f16 v[46:49], v[128:131], v[104:107], v[46:49]
	ds_read_b128 v[168:171], v94 offset:8192
	v_mfma_f32_16x16x32_f16 v[42:45], v[132:135], v[104:107], v[42:45]
	v_mfma_f32_16x16x32_f16 v[38:41], v[116:119], v[108:111], v[38:41]
	v_add_u32_e32 v91, s27, v89
	v_mfma_f32_16x16x32_f16 v[30:33], v[120:123], v[108:111], v[30:33]
	v_add_u32_e32 v93, s27, v90
	v_mfma_f32_16x16x32_f16 v[26:29], v[124:127], v[108:111], v[26:29]
	v_xor_b32_e32 v92, 64, v91
	v_mfma_f32_16x16x32_f16 v[22:25], v[128:131], v[108:111], v[22:25]
	v_xor_b32_e32 v94, 64, v93
	v_mfma_f32_16x16x32_f16 v[18:21], v[132:135], v[108:111], v[18:21]
	v_mfma_f32_16x16x32_f16 v[14:17], v[116:119], v[112:115], v[14:17]
	v_mfma_f32_16x16x32_f16 v[10:13], v[120:123], v[112:115], v[10:13]
	v_mfma_f32_16x16x32_f16 v[2:5], v[124:127], v[112:115], v[2:5]
	v_mfma_f32_16x16x32_f16 v[6:9], v[128:131], v[112:115], v[6:9]
	v_mfma_f32_16x16x32_f16 v[66:69], v[132:135], v[112:115], v[66:69]
	s_waitcnt vmcnt(0)
	s_waitcnt lgkmcnt(0)
	s_barrier
	v_mfma_f32_16x16x32_f16 v[34:37], v[152:155], v[136:139], v[34:37]
	ds_read_b128 v[116:119], v93
	v_mfma_f32_16x16x32_f16 v[78:81], v[156:159], v[136:139], v[78:81]
	ds_read_b128 v[100:103], v91
	v_mfma_f32_16x16x32_f16 v[74:77], v[160:163], v[136:139], v[74:77]
	ds_read_b128 v[120:123], v93 offset:2048
	v_mfma_f32_16x16x32_f16 v[70:73], v[164:167], v[136:139], v[70:73]
	ds_read_b128 v[104:107], v91 offset:2048
	v_mfma_f32_16x16x32_f16 v[62:65], v[168:171], v[136:139], v[62:65]
	ds_read_b128 v[124:127], v93 offset:4096
	v_mfma_f32_16x16x32_f16 v[58:61], v[152:155], v[140:143], v[58:61]
	ds_read_b128 v[108:111], v91 offset:4096
	v_mfma_f32_16x16x32_f16 v[54:57], v[156:159], v[140:143], v[54:57]
	ds_read_b128 v[128:131], v93 offset:6144
	v_mfma_f32_16x16x32_f16 v[50:53], v[160:163], v[140:143], v[50:53]
	ds_read_b128 v[112:115], v91 offset:6144
	v_mfma_f32_16x16x32_f16 v[46:49], v[164:167], v[140:143], v[46:49]
	ds_read_b128 v[132:135], v93 offset:8192
	v_mfma_f32_16x16x32_f16 v[42:45], v[168:171], v[140:143], v[42:45]
	v_mfma_f32_16x16x32_f16 v[38:41], v[152:155], v[144:147], v[38:41]
	v_mfma_f32_16x16x32_f16 v[30:33], v[156:159], v[144:147], v[30:33]
	v_mfma_f32_16x16x32_f16 v[26:29], v[160:163], v[144:147], v[26:29]
	v_mfma_f32_16x16x32_f16 v[22:25], v[164:167], v[144:147], v[22:25]
	v_mfma_f32_16x16x32_f16 v[18:21], v[168:171], v[144:147], v[18:21]
	v_mfma_f32_16x16x32_f16 v[14:17], v[152:155], v[148:151], v[14:17]
	v_mfma_f32_16x16x32_f16 v[10:13], v[156:159], v[148:151], v[10:13]
	v_mfma_f32_16x16x32_f16 v[2:5], v[160:163], v[148:151], v[2:5]
	v_mfma_f32_16x16x32_f16 v[6:9], v[164:167], v[148:151], v[6:9]
	v_mfma_f32_16x16x32_f16 v[66:69], v[168:171], v[148:151], v[66:69]
	s_mov_b32 s17, s27
	s_add_i32 s16, s16, 1
	s_add_i32 s27, s17, 0xd000
	s_cmp_lg_u32 s27, 0x27000
	s_cselect_b32 s27, s27, 0
	s_waitcnt lgkmcnt(0)
	v_mfma_f32_16x16x32_f16 v[34:37], v[116:119], v[100:103], v[34:37]
	ds_read_b128 v[152:155], v94
	v_mfma_f32_16x16x32_f16 v[78:81], v[120:123], v[100:103], v[78:81]
	ds_read_b128 v[136:139], v92
	v_mfma_f32_16x16x32_f16 v[74:77], v[124:127], v[100:103], v[74:77]
	ds_read_b128 v[156:159], v94 offset:2048
	v_mfma_f32_16x16x32_f16 v[70:73], v[128:131], v[100:103], v[70:73]
	ds_read_b128 v[140:143], v92 offset:2048
	v_mfma_f32_16x16x32_f16 v[62:65], v[132:135], v[100:103], v[62:65]
	ds_read_b128 v[160:163], v94 offset:4096
	v_mfma_f32_16x16x32_f16 v[58:61], v[116:119], v[104:107], v[58:61]
	ds_read_b128 v[144:147], v92 offset:4096
	v_mfma_f32_16x16x32_f16 v[54:57], v[120:123], v[104:107], v[54:57]
	ds_read_b128 v[164:167], v94 offset:6144
	v_mfma_f32_16x16x32_f16 v[50:53], v[124:127], v[104:107], v[50:53]
	ds_read_b128 v[148:151], v92 offset:6144
	v_mfma_f32_16x16x32_f16 v[46:49], v[128:131], v[104:107], v[46:49]
	ds_read_b128 v[168:171], v94 offset:8192
	v_mfma_f32_16x16x32_f16 v[42:45], v[132:135], v[104:107], v[42:45]
	v_mfma_f32_16x16x32_f16 v[38:41], v[116:119], v[108:111], v[38:41]
	v_add_u32_e32 v91, s27, v89
	v_mfma_f32_16x16x32_f16 v[30:33], v[120:123], v[108:111], v[30:33]
	v_add_u32_e32 v93, s27, v90
	v_mfma_f32_16x16x32_f16 v[26:29], v[124:127], v[108:111], v[26:29]
	v_xor_b32_e32 v92, 64, v91
	v_mfma_f32_16x16x32_f16 v[22:25], v[128:131], v[108:111], v[22:25]
	v_xor_b32_e32 v94, 64, v93
	v_mfma_f32_16x16x32_f16 v[18:21], v[132:135], v[108:111], v[18:21]
	v_mfma_f32_16x16x32_f16 v[14:17], v[116:119], v[112:115], v[14:17]
	v_mfma_f32_16x16x32_f16 v[10:13], v[120:123], v[112:115], v[10:13]
	v_mfma_f32_16x16x32_f16 v[2:5], v[124:127], v[112:115], v[2:5]
	v_mfma_f32_16x16x32_f16 v[6:9], v[128:131], v[112:115], v[6:9]
	v_mfma_f32_16x16x32_f16 v[66:69], v[132:135], v[112:115], v[66:69]
	s_waitcnt lgkmcnt(0)
	s_barrier
	v_mfma_f32_16x16x32_f16 v[34:37], v[152:155], v[136:139], v[34:37]
	ds_read_b128 v[116:119], v93
	v_mfma_f32_16x16x32_f16 v[78:81], v[156:159], v[136:139], v[78:81]
	ds_read_b128 v[100:103], v91
	v_mfma_f32_16x16x32_f16 v[74:77], v[160:163], v[136:139], v[74:77]
	ds_read_b128 v[120:123], v93 offset:2048
	v_mfma_f32_16x16x32_f16 v[70:73], v[164:167], v[136:139], v[70:73]
	ds_read_b128 v[104:107], v91 offset:2048
	v_mfma_f32_16x16x32_f16 v[62:65], v[168:171], v[136:139], v[62:65]
	ds_read_b128 v[124:127], v93 offset:4096
	v_mfma_f32_16x16x32_f16 v[58:61], v[152:155], v[140:143], v[58:61]
	ds_read_b128 v[108:111], v91 offset:4096
	v_mfma_f32_16x16x32_f16 v[54:57], v[156:159], v[140:143], v[54:57]
	ds_read_b128 v[128:131], v93 offset:6144
	v_mfma_f32_16x16x32_f16 v[50:53], v[160:163], v[140:143], v[50:53]
	ds_read_b128 v[112:115], v91 offset:6144
	v_mfma_f32_16x16x32_f16 v[46:49], v[164:167], v[140:143], v[46:49]
	ds_read_b128 v[132:135], v93 offset:8192
	v_mfma_f32_16x16x32_f16 v[42:45], v[168:171], v[140:143], v[42:45]
	v_mfma_f32_16x16x32_f16 v[38:41], v[152:155], v[144:147], v[38:41]
	v_mfma_f32_16x16x32_f16 v[30:33], v[156:159], v[144:147], v[30:33]
	v_mfma_f32_16x16x32_f16 v[26:29], v[160:163], v[144:147], v[26:29]
	v_mfma_f32_16x16x32_f16 v[22:25], v[164:167], v[144:147], v[22:25]
	v_mfma_f32_16x16x32_f16 v[18:21], v[168:171], v[144:147], v[18:21]
	v_mfma_f32_16x16x32_f16 v[14:17], v[152:155], v[148:151], v[14:17]
	v_mfma_f32_16x16x32_f16 v[10:13], v[156:159], v[148:151], v[10:13]
	v_mfma_f32_16x16x32_f16 v[2:5], v[160:163], v[148:151], v[2:5]
	v_mfma_f32_16x16x32_f16 v[6:9], v[164:167], v[148:151], v[6:9]
	v_mfma_f32_16x16x32_f16 v[66:69], v[168:171], v[148:151], v[66:69]
	s_mov_b32 s17, s27
	s_add_i32 s16, s16, 1
	s_nop 7

_Z8gemm_f16ILi128ELi64ELi2ELi2ELi4ELi2ELi0EEvPKDF16_S1_Pviiii:
	s_load_dwordx4 s[4:7], s[0:1], 0x0
	s_load_dwordx2 s[8:9], s[0:1], 0x10
	s_and_b32 s3, s2, 7
	s_lshr_b32 s10, s2, 3
	s_lshr_b32 s11, s3, 1
	s_lshl_b32 s11, s11, 2
	s_and_b32 s12, s10, 3
	s_and_b32 s3, s3, 1
	s_lshl_b32 s3, s3, 3
	s_lshr_b32 s10, s10, 2
	s_add_i32 s10, s10, s3
	s_add_i32 s3, s11, s12
	s_mov_b32 s11, s10
	s_lshl_b32 s10, s3, 7
	s_lshl_b32 s11, s11, 6
	v_lshrrev_b32_e32 v13, 3, v0
	v_and_b32_e32 v14, 7, v0
	v_bfe_u32 v15, v0, 4, 3
	v_xor_b32_e32 v14, v14, v15
	v_lshlrev_b32_e32 v14, 4, v14
	v_add_u32_e32 v15, s10, v13
	v_mul_u32_u24_e32 v15, 0xc00, v15
	v_add_u32_e32 v3, v15, v14
	v_add_u32_e32 v4, 0x18000, v3
	v_add_u32_e32 v5, 0x30000, v3
	v_add_u32_e32 v6, 0x48000, v3
	v_add_u32_e32 v15, s11, v13
	v_mul_u32_u24_e32 v15, 0xc00, v15
	v_add_u32_e32 v7, v15, v14
	v_add_u32_e32 v8, 0x18000, v7
	v_lshlrev_b32_e32 v13, 4, v0
	s_nop 0
	v_readfirstlane_b32 s20, v13
	v_and_b32_e32 v13, 15, v0
	v_bfe_u32 v14, v0, 4, 2
	v_bfe_u32 v15, v0, 1, 3
	v_xor_b32_e32 v14, v14, v15
	v_lshlrev_b32_e32 v14, 4, v14
	v_lshl_or_b32 v14, v13, 7, v14
	v_lshrrev_b32_e32 v13, 7, v0
	v_lshl_or_b32 v1, v13, 13, v14
	v_bfe_u32 v13, v0, 6, 1
	v_lshlrev_b32_e32 v13, 12, v13
	v_or_b32_e32 v13, 0x4000, v13
	v_or_b32_e32 v2, v13, v14
	s_waitcnt lgkmcnt(0)
	s_mov_b32 s14, s4
	s_mov_b32 s15, s5
	s_mov_b32 s16, s6
	s_mov_b32 s17, s7
	s_mov_b32 s21, s20
	s_mov_b32 m0, s21
	s_add_i32 s21, s21, 0x1000
	global_load_lds_dwordx4 v3, s[14:15]
	s_mov_b32 m0, s21
	s_add_i32 s21, s21, 0x1000
	global_load_lds_dwordx4 v4, s[14:15]
	s_mov_b32 m0, s21
	s_add_i32 s21, s21, 0x1000
	global_load_lds_dwordx4 v5, s[14:15]
	s_mov_b32 m0, s21
	s_add_i32 s21, s21, 0x1000
	global_load_lds_dwordx4 v6, s[14:15]
	s_mov_b32 m0, s21
	s_add_i32 s21, s21, 0x1000
	global_load_lds_dwordx4 v7, s[16:17]
	s_mov_b32 m0, s21
	s_add_i32 s21, s21, 0x1000
	global_load_lds_dwordx4 v8, s[16:17]
	s_add_u32 s14, s14, 0x80
	s_addc_u32 s15, s15, 0
	s_add_u32 s16, s16, 0x80
	s_addc_u32 s17, s17, 0
	s_mov_b32 m0, s21
	s_add_i32 s21, s21, 0x1000
	global_load_lds_dwordx4 v3, s[14:15]
	s_mov_b32 m0, s21
	s_add_i32 s21, s21, 0x1000
	global_load_lds_dwordx4 v4, s[14:15]
	s_mov_b32 m0, s21
	s_add_i32 s21, s21, 0x1000
	global_load_lds_dwordx4 v5, s[14:15]
	s_mov_b32 m0, s21
	s_add_i32 s21, s21, 0x1000
	global_load_lds_dwordx4 v6, s[14:15]
	s_mov_b32 m0, s21
	s_add_i32 s21, s21, 0x1000
	global_load_lds_dwordx4 v7, s[16:17]
	s_mov_b32 m0, s21
	s_add_i32 s21, s21, 0x1000
	global_load_lds_dwordx4 v8, s[16:17]
	s_add_u32 s14, s14, 0x80
	s_addc_u32 s15, s15, 0
	s_add_u32 s16, s16, 0x80
	s_addc_u32 s17, s17, 0
	s_mov_b32 m0, s21
	s_add_i32 s21, s21, 0x1000
	global_load_lds_dwordx4 v3, s[14:15]
	s_mov_b32 m0, s21
	s_add_i32 s21, s21, 0x1000
	global_load_lds_dwordx4 v4, s[14:15]
	s_mov_b32 m0, s21
	s_add_i32 s21, s21, 0x1000
	global_load_lds_dwordx4 v5, s[14:15]
	s_mov_b32 m0, s21
	s_add_i32 s21, s21, 0x1000
	global_load_lds_dwordx4 v6, s[14:15]
	s_mov_b32 m0, s21
	s_add_i32 s21, s21, 0x1000
	global_load_lds_dwordx4 v7, s[16:17]
	s_mov_b32 m0, s21
	s_add_i32 s21, s21, 0x1000
	global_load_lds_dwordx4 v8, s[16:17]
	s_add_u32 s14, s14, 0x80
	s_addc_u32 s15, s15, 0
	s_add_u32 s16, s16, 0x80
	s_addc_u32 s17, s17, 0
	s_mov_b32 m0, s21
	s_add_i32 s21, s21, 0x1000
	global_load_lds_dwordx4 v3, s[14:15]
	s_mov_b32 m0, s21
	s_add_i32 s21, s21, 0x1000
	global_load_lds_dwordx4 v4, s[14:15]
	s_mov_b32 m0, s21
	s_add_i32 s21, s21, 0x1000
	global_load_lds_dwordx4 v5, s[14:15]
	s_mov_b32 m0, s21
	s_add_i32 s21, s21, 0x1000
	global_load_lds_dwordx4 v6, s[14:15]
	s_mov_b32 m0, s21
	s_add_i32 s21, s21, 0x1000
	global_load_lds_dwordx4 v7, s[16:17]
	s_mov_b32 m0, s21
	s_add_i32 s21, s21, 0x1000
	global_load_lds_dwordx4 v8, s[16:17]
	v_accvgpr_write_b32 a0, 0
	v_accvgpr_write_b32 a1, 0
	v_accvgpr_write_b32 a2, 0
	v_accvgpr_write_b32 a3, 0
	v_accvgpr_write_b32 a4, 0
	v_accvgpr_write_b32 a5, 0
	v_accvgpr_write_b32 a6, 0
	v_accvgpr_write_b32 a7, 0
	v_accvgpr_write_b32 a8, 0
	v_accvgpr_write_b32 a9, 0
	v_accvgpr_write_b32 a10, 0
	v_accvgpr_write_b32 a11, 0
	v_accvgpr_write_b32 a12, 0
	v_accvgpr_write_b32 a13, 0
	v_accvgpr_write_b32 a14, 0
	v_accvgpr_write_b32 a15, 0
	v_accvgpr_write_b32 a16, 0
	v_accvgpr_write_b32 a17, 0
	v_accvgpr_write_b32 a18, 0
	v_accvgpr_write_b32 a19, 0
	v_accvgpr_write_b32 a20, 0
	v_accvgpr_write_b32 a21, 0
	v_accvgpr_write_b32 a22, 0
	v_accvgpr_write_b32 a23, 0
	v_accvgpr_write_b32 a24, 0
	v_accvgpr_write_b32 a25, 0
	v_accvgpr_write_b32 a26, 0
	v_accvgpr_write_b32 a27, 0
	v_accvgpr_write_b32 a28, 0
	v_accvgpr_write_b32 a29, 0
	v_accvgpr_write_b32 a30, 0
	v_accvgpr_write_b32 a31, 0
	s_mov_b32 s12, 0
	s_mov_b32 s13, 0
	v_mov_b32_e32 v9, v1
	v_mov_b32_e32 v11, v2
	v_xor_b32_e32 v10, 64, v1
	v_xor_b32_e32 v12, 64, v2
	s_waitcnt vmcnt(18)
	s_barrier
	ds_read_b128 v[16:19], v11
	ds_read_b128 v[24:27], v9
	ds_read_b128 v[20:23], v11 offset:2048
	ds_read_b128 v[28:31], v9 offset:2048
	ds_read_b128 v[32:35], v9 offset:4096
	ds_read_b128 v[36:39], v9 offset:6144
	s_add_i32 s23, s13, 0x6000
	s_cmp_lg_u32 s23, 0x18000
	s_cselect_b32 s23, s23, 0
	s_waitcnt lgkmcnt(0)
	v_mfma_f32_16x16x32_f16 a[0:3], v[16:19], v[24:27], a[0:3]
	ds_read_b128 v[40:43], v12
	v_mfma_f32_16x16x32_f16 a[4:7], v[20:23], v[24:27], a[4:7]
	ds_read_b128 v[48:51], v10
	v_mfma_f32_16x16x32_f16 a[8:11], v[16:19], v[28:31], a[8:11]
	ds_read_b128 v[44:47], v12 offset:2048
	v_mfma_f32_16x16x32_f16 a[12:15], v[20:23], v[28:31], a[12:15]
	ds_read_b128 v[52:55], v10 offset:2048
	v_mfma_f32_16x16x32_f16 a[16:19], v[16:19], v[32:35], a[16:19]
	ds_read_b128 v[56:59], v10 offset:4096
	v_mfma_f32_16x16x32_f16 a[20:23], v[20:23], v[32:35], a[20:23]
	ds_read_b128 v[60:63], v10 offset:6144
	v_mfma_f32_16x16x32_f16 a[24:27], v[16:19], v[36:39], a[24:27]
	v_add_u32_e32 v9, s23, v1
	v_add_u32_e32 v11, s23, v2
	v_mfma_f32_16x16x32_f16 a[28:31], v[20:23], v[36:39], a[28:31]
	v_xor_b32_e32 v10, 64, v9
	v_xor_b32_e32 v12, 64, v11
	s_add_i32 s22, s12, 4
	s_lshl_b32 s22, s22, 7
	s_add_u32 s14, s4, s22
	s_addc_u32 s15, s5, 0
	s_add_u32 s16, s6, s22
	s_addc_u32 s17, s7, 0
	s_add_i32 s21, s13, s20
	s_waitcnt vmcnt(12)
	s_waitcnt lgkmcnt(0)
	s_barrier
	v_mfma_f32_16x16x32_f16 a[0:3], v[40:43], v[48:51], a[0:3]
	ds_read_b128 v[16:19], v11
	v_mfma_f32_16x16x32_f16 a[4:7], v[44:47], v[48:51], a[4:7]
	ds_read_b128 v[24:27], v9
	s_mov_b32 m0, s21
	s_add_i32 s21, s21, 0x1000
	global_load_lds_dwordx4 v3, s[14:15]
	v_mfma_f32_16x16x32_f16 a[8:11], v[40:43], v[52:55], a[8:11]
	ds_read_b128 v[20:23], v11 offset:2048
	v_mfma_f32_16x16x32_f16 a[12:15], v[44:47], v[52:55], a[12:15]
	ds_read_b128 v[28:31], v9 offset:2048
	s_mov_b32 m0, s21
	s_add_i32 s21, s21, 0x1000
	global_load_lds_dwordx4 v4, s[14:15]
	v_mfma_f32_16x16x32_f16 a[16:19], v[40:43], v[56:59], a[16:19]
	ds_read_b128 v[32:35], v9 offset:4096
	v_mfma_f32_16x16x32_f16 a[20:23], v[44:47], v[56:59], a[20:23]
	ds_read_b128 v[36:39], v9 offset:6144
	s_mov_b32 m0, s21
	s_add_i32 s21, s21, 0x1000
	global_load_lds_dwordx4 v5, s[14:15]
	v_mfma_f32_16x16x32_f16 a[24:27], v[40:43], v[60:63], a[24:27]
	v_mfma_f32_16x16x32_f16 a[28:31], v[44:47], v[60:63], a[28:31]
	s_mov_b32 m0, s21
	s_add_i32 s21, s21, 0x1000
	global_load_lds_dwordx4 v6, s[14:15]
	s_mov_b32 s13, s23
	s_add_i32 s12, s12, 1
.Lg2_loop:
	s_add_i32 s23, s13, 0x6000
	s_cmp_lg_u32 s23, 0x18000
	s_cselect_b32 s23, s23, 0
	s_waitcnt lgkmcnt(0)
	v_mfma_f32_16x16x32_f16 a[0:3], v[16:19], v[24:27], a[0:3]
	ds_read_b128 v[40:43], v12
	v_mfma_f32_16x16x32_f16 a[4:7], v[20:23], v[24:27], a[4:7]
	ds_read_b128 v[48:51], v10
	v_mfma_f32_16x16x32_f16 a[8:11], v[16:19], v[28:31], a[8:11]
	ds_read_b128 v[44:47], v12 offset:2048
	v_mfma_f32_16x16x32_f16 a[12:15], v[20:23], v[28:31], a[12:15]
	ds_read_b128 v[52:55], v10 offset:2048
	s_mov_b32 m0, s21
	s_add_i32 s21, s21, 0x1000
	global_load_lds_dwordx4 v7, s[16:17]
	v_mfma_f32_16x16x32_f16 a[16:19], v[16:19], v[32:35], a[16:19]
	ds_read_b128 v[56:59], v10 offset:4096
	v_mfma_f32_16x16x32_f16 a[20:23], v[20:23], v[32:35], a[20:23]
	ds_read_b128 v[60:63], v10 offset:6144
	v_mfma_f32_16x16x32_f16 a[24:27], v[16:19], v[36:39], a[24:27]
	v_add_u32_e32 v9, s23, v1
	v_add_u32_e32 v11, s23, v2
	s_mov_b32 m0, s21
	s_nop 0
	global_load_lds_dwordx4 v8, s[16:17]
	v_mfma_f32_16x16x32_f16 a[28:31], v[20:23], v[36:39], a[28:31]
	v_xor_b32_e32 v10, 64, v9
	v_xor_b32_e32 v12, 64, v11
	s_add_i32 s22, s12, 4
	s_lshl_b32 s22, s22, 7
	s_add_u32 s14, s4, s22
	s_addc_u32 s15, s5, 0
	s_add_u32 s16, s6, s22
	s_addc_u32 s17, s7, 0
	s_add_i32 s21, s13, s20
	s_waitcnt vmcnt(12)
	s_waitcnt lgkmcnt(0)
	s_barrier
	v_mfma_f32_16x16x32_f16 a[0:3], v[40:43], v[48:51], a[0:3]
	ds_read_b128 v[16:19], v11
	v_mfma_f32_16x16x32_f16 a[4:7], v[44:47], v[48:51], a[4:7]
	ds_read_b128 v[24:27], v9
	s_mov_b32 m0, s21
	s_add_i32 s21, s21, 0x1000
	global_load_lds_dwordx4 v3, s[14:15]
	v_mfma_f32_16x16x32_f16 a[8:11], v[40:43], v[52:55], a[8:11]
	ds_read_b128 v[20:23], v11 offset:2048
	v_mfma_f32_16x16x32_f16 a[12:15], v[44:47], v[52:55], a[12:15]
	ds_read_b128 v[28:31], v9 offset:2048
	s_mov_b32 m0, s21
	s_add_i32 s21, s21, 0x1000
	global_load_lds_dwordx4 v4, s[14:15]
	v_mfma_f32_16x16x32_f16 a[16:19], v[40:43], v[56:59], a[16:19]
	ds_read_b128 v[32:35], v9 offset:4096
	v_mfma_f32_16x16x32_f16 a[20:23], v[44:47], v[56:59], a[20:23]
	ds_read_b128 v[36:39], v9 offset:6144
	s_mov_b32 m0, s21
	s_add_i32 s21, s21, 0x1000
	global_load_lds_dwordx4 v5, s[14:15]
	v_mfma_f32_16x16x32_f16 a[24:27], v[40:43], v[60:63], a[24:27]
	v_mfma_f32_16x16x32_f16 a[28:31], v[44:47], v[60:63], a[28:31]
	s_mov_b32 m0, s21
	s_add_i32 s21, s21, 0x1000
	global_load_lds_dwordx4 v6, s[14:15]
	s_mov_b32 s13, s23
	s_add_i32 s12, s12, 1
	s_cmp_lt_u32 s12, 20
	s_cbranch_scc1 .Lg2_loop
	s_add_i32 s23, s13, 0x6000
	s_cmp_lg_u32 s23, 0x18000
	s_cselect_b32 s23, s23, 0
	s_waitcnt lgkmcnt(0)
	v_mfma_f32_16x16x32_f16 a[0:3], v[16:19], v[24:27], a[0:3]
	ds_read_b128 v[40:43], v12
	v_mfma_f32_16x16x32_f16 a[4:7], v[20:23], v[24:27], a[4:7]
	ds_read_b128 v[48:51], v10
	v_mfma_f32_16x16x32_f16 a[8:11], v[16:19], v[28:31], a[8:11]
	ds_read_b128 v[44:47], v12 offset:2048
	v_mfma_f32_16x16x32_f16 a[12:15], v[20:23], v[28:31], a[12:15]
	ds_read_b128 v[52:55], v10 offset:2048
	s_mov_b32 m0, s21
	s_add_i32 s21, s21, 0x1000
	global_load_lds_dwordx4 v7, s[16:17]
	v_mfma_f32_16x16x32_f16 a[16:19], v[16:19], v[32:35], a[16:19]
	ds_read_b128 v[56:59], v10 offset:4096
	v_mfma_f32_16x16x32_f16 a[20:23], v[20:23], v[32:35], a[20:23]
	ds_read_b128 v[60:63], v10 offset:6144
	v_mfma_f32_16x16x32_f16 a[24:27], v[16:19], v[36:39], a[24:27]
	v_add_u32_e32 v9, s23, v1
	v_add_u32_e32 v11, s23, v2
	s_mov_b32 m0, s21
	s_nop 0
	global_load_lds_dwordx4 v8, s[16:17]
	v_mfma_f32_16x16x32_f16 a[28:31], v[20:23], v[36:39], a[28:31]
	v_xor_b32_e32 v10, 64, v9
	v_xor_b32_e32 v12, 64, v11
	s_waitcnt vmcnt(12)
	s_waitcnt lgkmcnt(0)
	s_barrier
	v_mfma_f32_16x16x32_f16 a[0:3], v[40:43], v[48:51], a[0:3]
	ds_read_b128 v[16:19], v11
	v_mfma_f32_16x16x32_f16 a[4:7], v[44:47], v[48:51], a[4:7]
	ds_read_b128 v[24:27], v9
	v_mfma_f32_16x16x32_f16 a[8:11], v[40:43], v[52:55], a[8:11]
	ds_read_b128 v[20:23], v11 offset:2048
	v_mfma_f32_16x16x32_f16 a[12:15], v[44:47], v[52:55], a[12:15]
	ds_read_b128 v[28:31], v9 offset:2048
	v_mfma_f32_16x16x32_f16 a[16:19], v[40:43], v[56:59], a[16:19]
	ds_read_b128 v[32:35], v9 offset:4096
	v_mfma_f32_16x16x32_f16 a[20:23], v[44:47], v[56:59], a[20:23]
	ds_read_b128 v[36:39], v9 offset:6144
	v_mfma_f32_16x16x32_f16 a[24:27], v[40:43], v[60:63], a[24:27]
	v_mfma_f32_16x16x32_f16 a[28:31], v[44:47], v[60:63], a[28:31]
	s_mov_b32 s13, s23
	s_add_i32 s12, s12, 1
	s_add_i32 s23, s13, 0x6000
	s_cmp_lg_u32 s23, 0x18000
	s_cselect_b32 s23, s23, 0
	s_waitcnt lgkmcnt(0)
	v_mfma_f32_16x16x32_f16 a[0:3], v[16:19], v[24:27], a[0:3]
	ds_read_b128 v[40:43], v12
	v_mfma_f32_16x16x32_f16 a[4:7], v[20:23], v[24:27], a[4:7]
	ds_read_b128 v[48:51], v10
	v_mfma_f32_16x16x32_f16 a[8:11], v[16:19], v[28:31], a[8:11]
	ds_read_b128 v[44:47], v12 offset:2048
	v_mfma_f32_16x16x32_f16 a[12:15], v[20:23], v[28:31], a[12:15]
	ds_read_b128 v[52:55], v10 offset:2048
	v_mfma_f32_16x16x32_f16 a[16:19], v[16:19], v[32:35], a[16:19]
	ds_read_b128 v[56:59], v10 offset:4096
	v_mfma_f32_16x16x32_f16 a[20:23], v[20:23], v[32:35], a[20:23]
	ds_read_b128 v[60:63], v10 offset:6144
	v_mfma_f32_16x16x32_f16 a[24:27], v[16:19], v[36:39], a[24:27]
	v_add_u32_e32 v9, s23, v1
	v_add_u32_e32 v11, s23, v2
	v_mfma_f32_16x16x32_f16 a[28:31], v[20:23], v[36:39], a[28:31]
	v_xor_b32_e32 v10, 64, v9
	v_xor_b32_e32 v12, 64, v11
	s_waitcnt vmcnt(6)
	s_waitcnt lgkmcnt(0)
	s_barrier
	v_mfma_f32_16x16x32_f16 a[0:3], v[40:43], v[48:51], a[0:3]
	ds_read_b128 v[16:19], v11
	v_mfma_f32_16x16x32_f16 a[4:7], v[44:47], v[48:51], a[4:7]
	ds_read_b128 v[24:27], v9
	v_mfma_f32_16x16x32_f16 a[8:11], v[40:43], v[52:55], a[8:11]
	ds_read_b128 v[20:23], v11 offset:2048
	v_mfma_f32_16x16x32_f16 a[12:15], v[44:47], v[52:55], a[12:15]
	ds_read_b128 v[28:31], v9 offset:2048
	v_mfma_f32_16x16x32_f16 a[16:19], v[40:43], v[56:59], a[16:19]
	ds_read_b128 v[32:35], v9 offset:4096
	v_mfma_f32_16x16x32_f16 a[20:23], v[44:47], v[56:59], a[20:23]
	ds_read_b128 v[36:39], v9 offset:6144
	v_mfma_f32_16x16x32_f16 a[24:27], v[40:43], v[60:63], a[24:27]
	v_mfma_f32_16x16x32_f16 a[28:31], v[44:47], v[60:63], a[28:31]
	s_mov_b32 s13, s23
	s_add_i32 s12, s12, 1
	s_add_i32 s23, s13, 0x6000
	s_cmp_lg_u32 s23, 0x18000
	s_cselect_b32 s23, s23, 0
	s_waitcnt lgkmcnt(0)
	v_mfma_f32_16x16x32_f16 a[0:3], v[16:19], v[24:27], a[0:3]
	ds_read_b128 v[40:43], v12
	v_mfma_f32_16x16x32_f16 a[4:7], v[20:23], v[24:27], a[4:7]
	ds_read_b128 v[48:51], v10
	v_mfma_f32_16x16x32_f16 a[8:11], v[16:19], v[28:31], a[8:11]
	ds_read_b128 v[44:47], v12 offset:2048
	v_mfma_f32_16x16x32_f16 a[12:15], v[20:23], v[28:31], a[12:15]
	ds_read_b128 v[52:55], v10 offset:2048
	v_mfma_f32_16x16x32_f16 a[16:19], v[16:19], v[32:35], a[16:19]
	ds_read_b128 v[56:59], v10 offset:4096
	v_mfma_f32_16x16x32_f16 a[20:23], v[20:23], v[32:35], a[20:23]
	ds_read_b128 v[60:63], v10 offset:6144
	v_mfma_f32_16x16x32_f16 a[24:27], v[16:19], v[36:39], a[24:27]
	v_add_u32_e32 v9, s23, v1
	v_add_u32_e32 v11, s23, v2
	v_mfma_f32_16x16x32_f16 a[28:31], v[20:23], v[36:39], a[28:31]
	v_xor_b32_e32 v10, 64, v9
	v_xor_b32_e32 v12, 64, v11
	s_waitcnt vmcnt(0)
	s_waitcnt lgkmcnt(0)
	s_barrier
	v_mfma_f32_16x16x32_f16 a[0:3], v[40:43], v[48:51], a[0:3]
	ds_read_b128 v[16:19], v11
	v_mfma_f32_16x16x32_f16 a[4:7], v[44:47], v[48:51], a[4:7]
	ds_read_b128 v[24:27], v9
	v_mfma_f32_16x16x32_f16 a[8:11], v[40:43], v[52:55], a[8:11]
	ds_read_b128 v[20:23], v11 offset:2048
	v_mfma_f32_16x16x32_f16 a[12:15], v[44:47], v[52:55], a[12:15]
	ds_read_b128 v[28:31], v9 offset:2048
	v_mfma_f32_16x16x32_f16 a[16:19], v[40:43], v[56:59], a[16:19]
	ds_read_b128 v[32:35], v9 offset:4096
	v_mfma_f32_16x16x32_f16 a[20:23], v[44:47], v[56:59], a[20:23]
	ds_read_b128 v[36:39], v9 offset:6144
	v_mfma_f32_16x16x32_f16 a[24:27], v[40:43], v[60:63], a[24:27]
	v_mfma_f32_16x16x32_f16 a[28:31], v[44:47], v[60:63], a[28:31]
	s_mov_b32 s13, s23
	s_add_i32 s12, s12, 1
	s_add_i32 s23, s13, 0x6000
	s_cmp_lg_u32 s23, 0x18000
	s_cselect_b32 s23, s23, 0
	s_waitcnt lgkmcnt(0)
	v_mfma_f32_16x16x32_f16 a[0:3], v[16:19], v[24:27], a[0:3]
	ds_read_b128 v[40:43], v12
	v_mfma_f32_16x16x32_f16 a[4:7], v[20:23], v[24:27], a[4:7]
	ds_read_b128 v[48:51], v10
	v_mfma_f32_16x16x32_f16 a[8:11], v[16:19], v[28:31], a[8:11]
	ds_read_b128 v[44:47], v12 offset:2048
	v_mfma_f32_16x16x32_f16 a[12:15], v[20:23], v[28:31], a[12:15]
	ds_read_b128 v[52:55], v10 offset:2048
	v_mfma_f32_16x16x32_f16 a[16:19], v[16:19], v[32:35], a[16:19]
	ds_read_b128 v[56:59], v10 offset:4096
	v_mfma_f32_16x16x32_f16 a[20:23], v[20:23], v[32:35], a[20:23]
	ds_read_b128 v[60:63], v10 offset:6144
	v_mfma_f32_16x16x32_f16 a[24:27], v[16:19], v[36:39], a[24:27]
	v_add_u32_e32 v9, s23, v1
	v_add_u32_e32 v11, s23, v2
	v_mfma_f32_16x16x32_f16 a[28:31], v[20:23], v[36:39], a[28:31]
	v_xor_b32_e32 v10, 64, v9
	v_xor_b32_e32 v12, 64, v11
	s_waitcnt lgkmcnt(0)
	s_barrier
	v_mfma_f32_16x16x32_f16 a[0:3], v[40:43], v[48:51], a[0:3]
	ds_read_b128 v[16:19], v11
	v_mfma_f32_16x16x32_f16 a[4:7], v[44:47], v[48:51], a[4:7]
	ds_read_b128 v[24:27], v9
	v_mfma_f32_16x16x32_f16 a[8:11], v[40:43], v[52:55], a[8:11]
	ds_read_b128 v[20:23], v11 offset:2048
	v_mfma_f32_16x16x32_f16 a[12:15], v[44:47], v[52:55], a[12:15]
	ds_read_b128 v[28:31], v9 offset:2048
	v_mfma_f32_16x16x32_f16 a[16:19], v[40:43], v[56:59], a[16:19]
	ds_read_b128 v[32:35], v9 offset:4096
	v_mfma_f32_16x16x32_f16 a[20:23], v[44:47], v[56:59], a[20:23]
	ds_read_b128 v[36:39], v9 offset:6144
	v_mfma_f32_16x16x32_f16 a[24:27], v[40:43], v[60:63], a[24:27]
	v_mfma_f32_16x16x32_f16 a[28:31], v[44:47], v[60:63], a[28:31]
	s_mov_b32 s13, s23
	s_add_i32 s12, s12, 1
	s_waitcnt vmcnt(0) lgkmcnt(0)
	v_and_b32_e32 v13, 15, v0
	v_lshrrev_b32_e32 v14, 7, v0
	v_lshl_add_u32 v13, v14, 6, v13
	v_add_u32_e32 v13, s10, v13
	v_bfe_u32 v14, v0, 6, 1
	v_bfe_u32 v15, v0, 4, 2
	v_lshlrev_b32_e32 v14, 5, v14
	v_lshl_add_u32 v14, v15, 2, v14
	v_add_u32_e32 v14, s11, v14
	v_lshlrev_b32_e32 v13, 10, v13
	v_add_u32_e32 v13, v13, v14
	v_lshlrev_b32_e32 v13, 2, v13
	v_add_u32_e32 v14, 0x10000, v13
	v_add_u32_e32 v15, 0x20000, v13
	v_add_u32_e32 v16, 0x30000, v13
	s_nop 7
	global_store_dwordx4 v13, a[0:3], s[8:9]
	global_store_dwordx4 v13, a[4:7], s[8:9] offset:64
	global_store_dwordx4 v14, a[8:11], s[8:9]
	global_store_dwordx4 v14, a[12:15], s[8:9] offset:64
	global_store_dwordx4 v15, a[16:19], s[8:9]
	global_store_dwordx4 v15, a[20:23], s[8:9] offset:64
	global_store_dwordx4 v16, a[24:27], s[8:9]
	global_store_dwordx4 v16, a[28:31], s[8:9] offset:64
	s_endpgm
	.p2alignl 8, 3212836864
